# non-temporal (nt) policy on phase 10's sixteen row loads of x only (x is not read again before the next layer); phase 6 hint dropped (it slowed warm passes)
# baseline (speedup 1.0000x reference)
.LBB0_840:
	s_ashr_i32 s5, s4, 31
	s_lshl_b64 s[14:15], s[4:5], 13
	v_lshl_add_u64 v[2:3], v[72:73], 0, s[14:15]
	global_load_dwordx4 v[74:77], v[2:3], off nt
	global_load_dwordx4 v[78:81], v[2:3], off offset:1024 nt
	global_load_dwordx4 v[56:59], v[2:3], off offset:2048 nt
	global_load_dwordx4 v[52:55], v[2:3], off offset:3072 nt
	v_add_co_u32_e32 v2, vcc, s73, v2
	s_add_i32 s18, s4, s22
	s_nop 0
	v_addc_co_u32_e32 v3, vcc, 0, v3, vcc
	global_load_dwordx4 v[48:51], v[2:3], off nt
	global_load_dwordx4 v[44:47], v[2:3], off offset:1024 nt
	global_load_dwordx4 v[36:39], v[2:3], off offset:3072 nt
	global_load_dwordx4 v[40:43], v[2:3], off offset:2048 nt
	global_load_dwordx4 v[82:85], v[62:63], off
	s_cmp_lt_i32 s18, 0x8000
	s_cselect_b32 s14, s18, s4
	s_ashr_i32 s15, s14, 31
	s_lshl_b64 s[14:15], s[14:15], 13
	s_lshl_b64 s[4:5], s[4:5], 12
	v_lshl_add_u64 v[2:3], v[72:73], 0, s[14:15]
	s_add_u32 s4, s23, s4
	v_lshlrev_b32_e32 v61, 3, v60
	s_addc_u32 s5, s24, s5
	s_cmpk_gt_i32 s18, 0x7fff
	s_waitcnt vmcnt(0)
	v_mov_b32_e32 v6, v75
	v_mov_b32_e32 v7, v79
	v_mov_b32_e32 v10, v77
	v_mov_b32_e32 v11, v81
	v_mov_b32_e32 v4, v74
	v_mov_b32_e32 v5, v78
	v_mov_b32_e32 v8, v76
	v_mov_b32_e32 v9, v80
	v_pk_mul_f32 v[12:13], v[58:59], v[58:59]
	v_pk_mul_f32 v[14:15], v[56:57], v[56:57]
	v_pk_mul_f32 v[6:7], v[6:7], v[6:7]
	v_pk_mul_f32 v[10:11], v[10:11], v[10:11]
	v_pk_mov_b32 v[20:21], v[14:15], v[12:13] op_sel:[1,0]
	v_mov_b32_e32 v15, v13
	v_pk_fma_f32 v[4:5], v[4:5], v[4:5], v[6:7]
	v_pk_fma_f32 v[6:7], v[8:9], v[8:9], v[10:11]
	v_mul_f32_e32 v16, v53, v53
	v_mul_f32_e32 v18, v55, v55
	v_pk_add_f32 v[8:9], v[20:21], v[14:15]
	v_pk_add_f32 v[4:5], v[4:5], v[6:7]
	v_mul_f32_e32 v25, v48, v48
	v_mul_f32_e32 v27, v49, v49
	v_mul_f32_e32 v28, v50, v50
	v_mul_f32_e32 v29, v51, v51
	v_pk_fma_f32 v[12:13], v[52:53], v[52:53], v[16:17] op_sel_hi:[1,1,0]
	v_pk_fma_f32 v[16:17], v[54:55], v[54:55], v[18:19] op_sel_hi:[1,1,0]
	v_pk_add_f32 v[6:7], v[8:9], v[8:9] op_sel:[0,1] op_sel_hi:[1,0]
	v_pk_add_f32 v[4:5], v[4:5], v[4:5] op_sel:[0,1] op_sel_hi:[1,0]
	v_pk_mul_f32 v[18:19], v[46:47], v[46:47]
	v_pk_mul_f32 v[22:23], v[44:45], v[44:45]
	v_mov_b32_e32 v13, v28
	v_mov_b32_e32 v17, v29
	v_mov_b32_e32 v7, v27
	v_mov_b32_e32 v5, v25
	v_pk_mov_b32 v[10:11], v[22:23], v[18:19] op_sel:[1,0]
	v_mov_b32_e32 v23, v19
	v_pk_add_f32 v[8:9], v[12:13], v[16:17]
	v_pk_add_f32 v[4:5], v[4:5], v[6:7]
	v_mul_f32_e32 v24, v41, v41
	v_mul_f32_e32 v26, v43, v43
	v_pk_add_f32 v[10:11], v[10:11], v[22:23]
	v_pk_add_f32 v[4:5], v[4:5], v[8:9]
	v_mul_f32_e32 v30, v36, v36
	v_mul_f32_e32 v31, v37, v37
	v_mul_f32_e32 v32, v38, v38
	v_mul_f32_e32 v33, v39, v39
	v_pk_fma_f32 v[14:15], v[40:41], v[40:41], v[24:25] op_sel_hi:[1,1,0]
	v_pk_fma_f32 v[18:19], v[42:43], v[42:43], v[26:27] op_sel_hi:[1,1,0]
	v_pk_add_f32 v[10:11], v[10:11], v[10:11] op_sel:[0,1] op_sel_hi:[1,0]
	v_pk_add_f32 v[4:5], v[4:5], v[4:5] op_sel:[0,1] op_sel_hi:[1,0]
	v_mov_b32_e32 v15, v32
	v_mov_b32_e32 v19, v33
	v_mov_b32_e32 v11, v31
	v_mov_b32_e32 v5, v30
	v_pk_add_f32 v[12:13], v[14:15], v[18:19]
	v_pk_add_f32 v[4:5], v[4:5], v[10:11]
	global_load_dwordx4 v[30:33], v[2:3], off nt
	global_load_dwordx4 v[26:29], v[2:3], off offset:1024 nt
	global_load_dwordx4 v[22:25], v[2:3], off offset:2048 nt
	global_load_dwordx4 v[18:21], v[2:3], off offset:3072 nt
	v_pk_add_f32 v[4:5], v[4:5], v[12:13]
	v_add_co_u32_e32 v2, vcc, s73, v2
	v_add_f32_e32 v4, v4, v5
	s_nop 0
	v_addc_co_u32_e32 v3, vcc, 0, v3, vcc
	v_add_f32_dpp v4, v4, v4 quad_perm:[1,0,3,2] row_mask:0xf bank_mask:0xf bound_ctrl:1
	s_nop 1
	v_add_f32_dpp v4, v4, v4 quad_perm:[2,3,0,1] row_mask:0xf bank_mask:0xf bound_ctrl:1
	s_nop 1
	v_add_f32_dpp v4, v4, v4 row_half_mirror row_mask:0xf bank_mask:0xf bound_ctrl:1
	s_nop 1
	v_add_f32_dpp v4, v4, v4 row_mirror row_mask:0xf bank_mask:0xf bound_ctrl:1
	ds_swizzle_b32 v5, v4 offset:swizzle(SWAP,16)
	s_waitcnt lgkmcnt(0)
	v_add_f32_e32 v4, v4, v5
	ds_bpermute_b32 v5, v1, v4
	s_waitcnt lgkmcnt(0)
	v_add_f32_e32 v4, v4, v5
	v_fmamk_f32 v4, v4, 0x3a000000, v214
	v_rsq_f32_e32 v34, v4
	global_load_dwordx4 v[14:17], v[2:3], off nt
	global_load_dwordx4 v[10:13], v[2:3], off offset:1024 nt
	global_load_dwordx4 v[6:9], v[2:3], off offset:2048 nt
	s_nop 0
	global_load_dwordx4 v[2:5], v[2:3], off offset:3072 nt
	v_pk_mul_f32 v[74:75], v[74:75], v[34:35] op_sel_hi:[1,0]
	v_pk_mul_f32 v[76:77], v[76:77], v[34:35] op_sel_hi:[1,0]
	v_pk_mul_f32 v[74:75], v[82:83], v[74:75]
	v_pk_mul_f32 v[76:77], v[84:85], v[76:77]
	v_cvt_pk_bf16_f32 v74, v74, v75
	v_cvt_pk_bf16_f32 v75, v76, v77
	global_store_dwordx2 v61, v[74:75], s[4:5]
	global_load_dwordx4 v[74:77], v[62:63], off offset:1024
	v_pk_mul_f32 v[78:79], v[78:79], v[34:35] op_sel_hi:[1,0]
	v_pk_mul_f32 v[80:81], v[80:81], v[34:35] op_sel_hi:[1,0]
	v_pk_mul_f32 v[56:57], v[56:57], v[34:35] op_sel_hi:[1,0]
	v_pk_mul_f32 v[58:59], v[58:59], v[34:35] op_sel_hi:[1,0]
	v_pk_mul_f32 v[52:53], v[52:53], v[34:35] op_sel_hi:[1,0]
	v_pk_mul_f32 v[54:55], v[54:55], v[34:35] op_sel_hi:[1,0]
	v_pk_mul_f32 v[48:49], v[48:49], v[34:35] op_sel_hi:[1,0]
	v_pk_mul_f32 v[50:51], v[50:51], v[34:35] op_sel_hi:[1,0]
	v_pk_mul_f32 v[44:45], v[44:45], v[34:35] op_sel_hi:[1,0]
	v_pk_mul_f32 v[46:47], v[46:47], v[34:35] op_sel_hi:[1,0]
	v_pk_mul_f32 v[40:41], v[40:41], v[34:35] op_sel_hi:[1,0]
	v_pk_mul_f32 v[42:43], v[42:43], v[34:35] op_sel_hi:[1,0]
	v_pk_mul_f32 v[36:37], v[36:37], v[34:35] op_sel_hi:[1,0]
	v_pk_mul_f32 v[38:39], v[38:39], v[34:35] op_sel_hi:[1,0]
	s_waitcnt vmcnt(0)
	v_pk_mul_f32 v[74:75], v[74:75], v[78:79]
	v_pk_mul_f32 v[76:77], v[76:77], v[80:81]
	v_cvt_pk_bf16_f32 v74, v74, v75
	v_cvt_pk_bf16_f32 v75, v76, v77
	global_store_dwordx2 v61, v[74:75], s[4:5] offset:512
	global_load_dwordx4 v[74:77], v[62:63], off offset:2048
	s_waitcnt vmcnt(0)
	v_pk_mul_f32 v[56:57], v[74:75], v[56:57]
	v_pk_mul_f32 v[58:59], v[76:77], v[58:59]
	v_cvt_pk_bf16_f32 v56, v56, v57
	v_cvt_pk_bf16_f32 v57, v58, v59
	global_store_dwordx2 v61, v[56:57], s[4:5] offset:1024
	global_load_dwordx4 v[56:59], v[62:63], off offset:3072
	s_waitcnt vmcnt(0)
	v_pk_mul_f32 v[52:53], v[52:53], v[56:57]
	v_pk_mul_f32 v[54:55], v[54:55], v[58:59]
	v_cvt_pk_bf16_f32 v52, v52, v53
	v_cvt_pk_bf16_f32 v53, v54, v55
	global_store_dwordx2 v61, v[52:53], s[4:5] offset:1536
	global_load_dwordx4 v[52:55], v[64:65], off
	s_waitcnt vmcnt(0)
	v_pk_mul_f32 v[48:49], v[48:49], v[52:53]
	v_pk_mul_f32 v[50:51], v[50:51], v[54:55]
	v_cvt_pk_bf16_f32 v48, v48, v49
	v_cvt_pk_bf16_f32 v49, v50, v51
	global_store_dwordx2 v61, v[48:49], s[4:5] offset:2048
	global_load_dwordx4 v[48:51], v[66:67], off
	s_waitcnt vmcnt(0)
	v_pk_mul_f32 v[44:45], v[44:45], v[48:49]
	v_pk_mul_f32 v[46:47], v[46:47], v[50:51]
	v_cvt_pk_bf16_f32 v44, v44, v45
	v_cvt_pk_bf16_f32 v45, v46, v47
	global_store_dwordx2 v61, v[44:45], s[4:5] offset:2560
	global_load_dwordx4 v[44:47], v[68:69], off
	s_waitcnt vmcnt(0)
	v_pk_mul_f32 v[40:41], v[40:41], v[44:45]
	v_pk_mul_f32 v[42:43], v[42:43], v[46:47]
	v_cvt_pk_bf16_f32 v40, v40, v41
	v_cvt_pk_bf16_f32 v41, v42, v43
	global_store_dwordx2 v61, v[40:41], s[4:5] offset:3072
	global_load_dwordx4 v[40:43], v[70:71], off
	s_waitcnt vmcnt(0)
	v_pk_mul_f32 v[36:37], v[36:37], v[40:41]
	v_pk_mul_f32 v[38:39], v[38:39], v[42:43]
	v_cvt_pk_bf16_f32 v36, v36, v37
	v_cvt_pk_bf16_f32 v37, v38, v39
	global_store_dwordx2 v61, v[36:37], s[4:5] offset:3584
	s_cbranch_scc1 .LBB0_839
	v_mov_b32_e32 v38, v31
	v_mov_b32_e32 v39, v27
	v_mov_b32_e32 v36, v30
	v_mov_b32_e32 v37, v26
	v_pk_mul_f32 v[38:39], v[38:39], v[38:39]
	v_mov_b32_e32 v40, v33
	v_mov_b32_e32 v41, v29
	v_pk_fma_f32 v[36:37], v[36:37], v[36:37], v[38:39]
	v_mov_b32_e32 v38, v32
	v_mov_b32_e32 v39, v28
	v_pk_mul_f32 v[40:41], v[40:41], v[40:41]
	v_mul_f32_e32 v34, v14, v14
	v_pk_fma_f32 v[38:39], v[38:39], v[38:39], v[40:41]
	v_pk_mul_f32 v[40:41], v[22:23], v[22:23]
	v_pk_add_f32 v[36:37], v[36:37], v[38:39]
	v_pk_mul_f32 v[38:39], v[24:25], v[24:25]
	v_pk_add_f32 v[36:37], v[36:37], v[36:37] op_sel:[0,1] op_sel_hi:[1,0]
	v_pk_mov_b32 v[42:43], v[40:41], v[38:39] op_sel:[1,0]
	v_mov_b32_e32 v41, v39
	v_pk_add_f32 v[38:39], v[42:43], v[40:41]
	v_mul_f32_e32 v40, v15, v15
	v_pk_add_f32 v[38:39], v[38:39], v[38:39] op_sel:[0,1] op_sel_hi:[1,0]
	v_mov_b32_e32 v37, v34
	v_mov_b32_e32 v39, v40
	v_mul_f32_e32 v34, v19, v19
	v_mul_f32_e32 v41, v16, v16
	v_pk_add_f32 v[36:37], v[36:37], v[38:39]
	v_pk_fma_f32 v[38:39], v[18:19], v[18:19], v[34:35] op_sel_hi:[1,1,0]
	v_mul_f32_e32 v34, v21, v21
	v_mul_f32_e32 v42, v17, v17
	v_mov_b32_e32 v39, v41
	v_pk_fma_f32 v[40:41], v[20:21], v[20:21], v[34:35] op_sel_hi:[1,1,0]
	v_mul_f32_e32 v34, v2, v2
	v_mov_b32_e32 v41, v42
	v_pk_add_f32 v[38:39], v[38:39], v[40:41]
	v_pk_mul_f32 v[40:41], v[10:11], v[10:11]
	v_pk_add_f32 v[36:37], v[36:37], v[38:39]
	v_pk_mul_f32 v[38:39], v[12:13], v[12:13]
	v_pk_add_f32 v[36:37], v[36:37], v[36:37] op_sel:[0,1] op_sel_hi:[1,0]
	v_pk_mov_b32 v[42:43], v[40:41], v[38:39] op_sel:[1,0]
	v_mov_b32_e32 v41, v39
	v_pk_add_f32 v[38:39], v[42:43], v[40:41]
	v_mul_f32_e32 v40, v3, v3
	v_pk_add_f32 v[38:39], v[38:39], v[38:39] op_sel:[0,1] op_sel_hi:[1,0]
	v_mov_b32_e32 v37, v34
	v_mov_b32_e32 v39, v40
	v_mul_f32_e32 v34, v7, v7
	v_mul_f32_e32 v41, v4, v4
	v_pk_add_f32 v[36:37], v[36:37], v[38:39]
	v_pk_fma_f32 v[38:39], v[6:7], v[6:7], v[34:35] op_sel_hi:[1,1,0]
	v_mul_f32_e32 v34, v9, v9
	v_mul_f32_e32 v42, v5, v5
	v_mov_b32_e32 v39, v41
	v_pk_fma_f32 v[40:41], v[8:9], v[8:9], v[34:35] op_sel_hi:[1,1,0]
	s_ashr_i32 s19, s18, 31
	v_mov_b32_e32 v41, v42
	v_pk_add_f32 v[38:39], v[38:39], v[40:41]
	s_lshl_b64 s[4:5], s[18:19], 12
	v_pk_add_f32 v[36:37], v[36:37], v[38:39]
	s_add_u32 s20, s23, s4
	v_add_f32_e32 v34, v36, v37
	s_addc_u32 s21, s24, s5
	s_nop 0
	v_add_f32_dpp v34, v34, v34 quad_perm:[1,0,3,2] row_mask:0xf bank_mask:0xf bound_ctrl:1
	s_nop 1
	v_add_f32_dpp v34, v34, v34 quad_perm:[2,3,0,1] row_mask:0xf bank_mask:0xf bound_ctrl:1
	s_nop 1
	v_add_f32_dpp v34, v34, v34 row_half_mirror row_mask:0xf bank_mask:0xf bound_ctrl:1
	s_nop 1
	v_add_f32_dpp v34, v34, v34 row_mirror row_mask:0xf bank_mask:0xf bound_ctrl:1
	ds_swizzle_b32 v36, v34 offset:swizzle(SWAP,16)
	s_waitcnt lgkmcnt(0)
	v_add_f32_e32 v34, v34, v36
	ds_bpermute_b32 v36, v1, v34
	s_waitcnt lgkmcnt(0)
	v_add_f32_e32 v34, v34, v36
	global_load_dwordx4 v[36:39], v[62:63], off
	v_fmamk_f32 v34, v34, 0x3a000000, v214
	v_rsq_f32_e32 v34, v34
	s_nop 0
	v_pk_mul_f32 v[30:31], v[30:31], v[34:35] op_sel_hi:[1,0]
	v_pk_mul_f32 v[32:33], v[32:33], v[34:35] op_sel_hi:[1,0]
	v_pk_mul_f32 v[26:27], v[26:27], v[34:35] op_sel_hi:[1,0]
	v_pk_mul_f32 v[28:29], v[28:29], v[34:35] op_sel_hi:[1,0]
	v_pk_mul_f32 v[22:23], v[22:23], v[34:35] op_sel_hi:[1,0]
	v_pk_mul_f32 v[24:25], v[24:25], v[34:35] op_sel_hi:[1,0]
	v_pk_mul_f32 v[18:19], v[18:19], v[34:35] op_sel_hi:[1,0]
	v_pk_mul_f32 v[20:21], v[20:21], v[34:35] op_sel_hi:[1,0]
	v_pk_mul_f32 v[14:15], v[14:15], v[34:35] op_sel_hi:[1,0]
	v_pk_mul_f32 v[16:17], v[16:17], v[34:35] op_sel_hi:[1,0]
	v_pk_mul_f32 v[10:11], v[10:11], v[34:35] op_sel_hi:[1,0]
	v_pk_mul_f32 v[12:13], v[12:13], v[34:35] op_sel_hi:[1,0]
	v_pk_mul_f32 v[6:7], v[6:7], v[34:35] op_sel_hi:[1,0]
	v_pk_mul_f32 v[8:9], v[8:9], v[34:35] op_sel_hi:[1,0]
	v_pk_mul_f32 v[2:3], v[2:3], v[34:35] op_sel_hi:[1,0]
	v_pk_mul_f32 v[4:5], v[4:5], v[34:35] op_sel_hi:[1,0]
	s_waitcnt vmcnt(0)
	v_pk_mul_f32 v[30:31], v[36:37], v[30:31]
	v_pk_mul_f32 v[32:33], v[38:39], v[32:33]
	v_cvt_pk_bf16_f32 v30, v30, v31
	v_cvt_pk_bf16_f32 v31, v32, v33
	global_store_dwordx2 v61, v[30:31], s[20:21]
	global_load_dwordx4 v[30:33], v[62:63], off offset:1024
	s_waitcnt vmcnt(0)
	v_pk_mul_f32 v[26:27], v[30:31], v[26:27]
	v_pk_mul_f32 v[28:29], v[32:33], v[28:29]
	v_cvt_pk_bf16_f32 v26, v26, v27
	v_cvt_pk_bf16_f32 v27, v28, v29
	global_store_dwordx2 v61, v[26:27], s[20:21] offset:512
	global_load_dwordx4 v[26:29], v[62:63], off offset:2048
	s_waitcnt vmcnt(0)
	v_pk_mul_f32 v[22:23], v[26:27], v[22:23]
	v_pk_mul_f32 v[24:25], v[28:29], v[24:25]
	v_cvt_pk_bf16_f32 v22, v22, v23
	v_cvt_pk_bf16_f32 v23, v24, v25
	global_store_dwordx2 v61, v[22:23], s[20:21] offset:1024
	global_load_dwordx4 v[22:25], v[62:63], off offset:3072
	s_waitcnt vmcnt(0)
	v_pk_mul_f32 v[18:19], v[22:23], v[18:19]
	v_pk_mul_f32 v[20:21], v[24:25], v[20:21]
	v_cvt_pk_bf16_f32 v18, v18, v19
	v_cvt_pk_bf16_f32 v19, v20, v21
	global_store_dwordx2 v61, v[18:19], s[20:21] offset:1536
	global_load_dwordx4 v[18:21], v[64:65], off
	s_waitcnt vmcnt(0)
	v_pk_mul_f32 v[14:15], v[14:15], v[18:19]
	v_pk_mul_f32 v[16:17], v[16:17], v[20:21]
	v_cvt_pk_bf16_f32 v14, v14, v15
	v_cvt_pk_bf16_f32 v15, v16, v17
	global_store_dwordx2 v61, v[14:15], s[20:21] offset:2048
	global_load_dwordx4 v[14:17], v[66:67], off
	s_waitcnt vmcnt(0)
	v_pk_mul_f32 v[10:11], v[10:11], v[14:15]
	v_pk_mul_f32 v[12:13], v[12:13], v[16:17]
	v_cvt_pk_bf16_f32 v10, v10, v11
	v_cvt_pk_bf16_f32 v11, v12, v13
	global_store_dwordx2 v61, v[10:11], s[20:21] offset:2560
	global_load_dwordx4 v[10:13], v[68:69], off
	s_waitcnt vmcnt(0)
	v_pk_mul_f32 v[6:7], v[6:7], v[10:11]
	v_pk_mul_f32 v[8:9], v[8:9], v[12:13]
	v_cvt_pk_bf16_f32 v6, v6, v7
	v_cvt_pk_bf16_f32 v7, v8, v9
	global_store_dwordx2 v61, v[6:7], s[20:21] offset:3072
	global_load_dwordx4 v[6:9], v[70:71], off
	s_waitcnt vmcnt(0)
	v_pk_mul_f32 v[2:3], v[2:3], v[6:7]
	v_pk_mul_f32 v[4:5], v[4:5], v[8:9]
	v_cvt_pk_bf16_f32 v2, v2, v3
	v_cvt_pk_bf16_f32 v3, v4, v5
	global_store_dwordx2 v61, v[2:3], s[20:21] offset:3584
	s_branch .LBB0_839
